# v88 + bf16 in-proj rope epilogue: rope-table loads one row-group ahead into dead fragment registers v[172:187], exact vmcnt counts
# baseline (speedup 1.0000x reference)
.LBB0_3362:
	s_and_b64 s[4:5], s[6:7], exec
	s_cselect_b32 s4, s34, 0
	v_or_b32_e32 v132, s4, v250
	s_mov_b32 s4, 0x14e00000
	s_cselect_b32 s4, s4, 0x15600000
	s_add_u32 s62, s8, s4
	s_addc_u32 s63, s9, 0
	s_and_b64 s[4:5], s[6:7], exec
	v_lshlrev_b32_e32 v134, 3, v132
	v_mov_b32_e32 v135, v1
	v_cndmask_b32_e64 v131, 0, 1, s[64:65]
	s_cselect_b32 s66, 6, 5
	v_cmp_ne_u32_e64 s[4:5], 1, v131
	s_andn2_b64 vcc, exec, s[64:65]
	v_lshl_add_u64 v[134:135], s[62:63], 0, v[134:135]
	s_cbranch_vccnz .LBB0_3364
	v_ashrrev_i32_e32 v131, 31, v130
	v_lshlrev_b64 v[136:137], s66, v[130:131]
	v_lshl_add_u64 v[136:137], v[136:137], 3, v[134:135]
	global_load_dwordx4 v[158:161], v[136:137], off offset:48
	global_load_dwordx4 v[138:141], v[136:137], off offset:32
	global_load_dwordx4 v[142:145], v[136:137], off offset:16
	global_load_dwordx4 v[146:149], v[136:137], off
	v_add_u32_e32 v188, 0x10, v130
	v_ashrrev_i32_e32 v189, 31, v188
	v_lshlrev_b64 v[188:189], s66, v[188:189]
	v_lshl_add_u64 v[188:189], v[188:189], 3, v[134:135]
	global_load_dwordx4 v[172:175], v[188:189], off offset:48
	global_load_dwordx4 v[176:179], v[188:189], off offset:32
	global_load_dwordx4 v[180:183], v[188:189], off offset:16
	global_load_dwordx4 v[184:187], v[188:189], off
	s_add_i32 s98, s66, 7
	s_lshl_b32 s98, 1, s98
	s_mov_b32 s99, 0
	v_lshl_add_u64 v[210:211], v[136:137], 0, s[98:99]
	global_load_dword v212, v[210:211], off
	v_lshl_add_u64 v[210:211], v[210:211], 0, s[98:99]
	global_load_dword v212, v[210:211], off
	v_lshl_add_u64 v[210:211], v[210:211], 0, s[98:99]
	global_load_dword v212, v[210:211], off
	v_lshl_add_u64 v[210:211], v[210:211], 0, s[98:99]
	v_lshl_add_u64 v[210:211], v[210:211], 0, s[98:99]
	v_lshl_add_u64 v[210:211], v[210:211], 0, s[98:99]
	v_lshl_add_u64 v[210:211], v[210:211], 0, s[98:99]
	v_lshl_add_u64 v[210:211], v[210:211], 0, s[98:99]
	global_load_dword v212, v[210:211], off
	v_lshl_add_u64 v[210:211], v[210:211], 0, s[98:99]
	global_load_dword v212, v[210:211], off
	v_lshl_add_u64 v[210:211], v[210:211], 0, s[98:99]
	global_load_dword v212, v[210:211], off
	v_lshl_add_u64 v[210:211], v[210:211], 0, s[98:99]
	global_load_dword v212, v[210:211], off
	s_waitcnt vmcnt(11)
	v_mul_f32_e32 v164, v124, v158
	v_mov_b32_e32 v153, v140
	v_mov_b32_e32 v140, v139
	v_mov_b32_e32 v137, v148
	v_mov_b32_e32 v148, v147
	v_mov_b32_e32 v136, v146
	v_pk_mul_f32 v[162:163], v[118:119], v[148:149]
	v_pk_mul_f32 v[146:147], v[126:127], v[148:149]
	v_mov_b32_e32 v149, v144
	v_mov_b32_e32 v144, v143
	v_mov_b32_e32 v148, v142
	v_pk_mul_f32 v[142:143], v[120:121], v[144:145]
	v_pk_mul_f32 v[150:151], v[128:129], v[144:145]
	v_mov_b32_e32 v152, v138
	v_pk_mul_f32 v[138:139], v[114:115], v[140:141]
	v_pk_mul_f32 v[154:155], v[122:123], v[140:141]
	v_mov_b32_e32 v140, v125
	v_mov_b32_e32 v141, v117
	v_pk_fma_f32 v[144:145], v[126:127], v[136:137], v[162:163] neg_lo:[0,0,1] neg_hi:[0,0,1]
	v_mov_b32_e32 v162, v117
	v_mov_b32_e32 v163, v125
	v_pk_mul_f32 v[140:141], v[140:141], v[160:161]
	v_pk_mul_f32 v[160:161], v[162:163], v[160:161]
	v_mul_f32_e32 v166, v116, v159
	v_mul_f32_e32 v156, v116, v158
	v_mul_f32_e32 v158, v124, v159
	v_mov_b32_e32 v165, v140
	v_mov_b32_e32 v167, v141
	v_mov_b32_e32 v157, v160
	v_mov_b32_e32 v159, v161
	v_pk_fma_f32 v[142:143], v[128:129], v[148:149], v[142:143] neg_lo:[0,0,1] neg_hi:[0,0,1]
	v_pk_fma_f32 v[140:141], v[122:123], v[152:153], v[138:139] neg_lo:[0,0,1] neg_hi:[0,0,1]
	v_pk_add_f32 v[138:139], v[164:165], v[166:167] neg_lo:[0,1] neg_hi:[0,1]
	v_pk_fma_f32 v[160:161], v[118:119], v[136:137], v[146:147]
	v_pk_fma_f32 v[150:151], v[120:121], v[148:149], v[150:151]
	v_pk_fma_f32 v[148:149], v[114:115], v[152:153], v[154:155]
	v_pk_add_f32 v[146:147], v[156:157], v[158:159]
	s_branch .LBB0_3365

.LBB0_3369:
	v_pk_mul_f32 v[140:141], s[56:57], v[140:141] op_sel_hi:[0,1]
	v_pk_mul_f32 v[138:139], s[56:57], v[138:139] op_sel_hi:[0,1]
	v_pk_mul_f32 v[142:143], s[56:57], v[142:143] op_sel_hi:[0,1]
	v_cvt_pk_bf16_f32 v156, v140, v141
	v_cvt_pk_bf16_f32 v157, v138, v139
	v_pk_mul_f32 v[138:139], s[56:57], v[160:161] op_sel_hi:[0,1]
	v_pk_mul_f32 v[140:141], s[56:57], v[150:151] op_sel_hi:[0,1]
	s_and_b64 s[6:7], s[6:7], exec
	v_pk_mul_f32 v[144:145], s[56:57], v[144:145] op_sel_hi:[0,1]
	v_cvt_pk_bf16_f32 v155, v142, v143
	v_cvt_pk_bf16_f32 v138, v138, v139
	v_cvt_pk_bf16_f32 v139, v140, v141
	v_pk_mul_f32 v[140:141], s[56:57], v[148:149] op_sel_hi:[0,1]
	v_pk_mul_f32 v[142:143], s[56:57], v[146:147] op_sel_hi:[0,1]
	s_cselect_b32 s0, 64, 32
	v_cvt_pk_bf16_f32 v154, v144, v145
	v_cvt_pk_bf16_f32 v140, v140, v141
	v_cvt_pk_bf16_f32 v141, v142, v143
	v_lshl_add_u64 v[142:143], v[152:153], 1, s[54:55]
	s_lshl_b32 s92, s0, 1
	global_store_dwordx4 v[142:143], v[154:157], off
	v_lshl_add_u64 v[142:143], v[142:143], 0, s[92:93]
	global_store_dwordx4 v[142:143], v[138:141], off
	s_and_b64 vcc, exec, s[4:5]
	s_nop 0
	v_or_b32_e32 v138, 16, v130
	v_ashrrev_i32_e32 v139, 31, v138
	s_cbranch_vccnz .LBB0_3371
	v_lshlrev_b64 v[140:141], s66, v[138:139]
	v_lshl_add_u64 v[140:141], v[140:141], 3, v[134:135]
	v_mov_b32_e32 v160, v109
	v_mov_b32_e32 v161, v101
	s_waitcnt vmcnt(9)
	v_mov_b64_e32 v[162:163], v[172:173]
	v_mov_b64_e32 v[164:165], v[174:175]
	v_mov_b64_e32 v[150:151], v[176:177]
	v_mov_b64_e32 v[152:153], v[178:179]
	v_mov_b64_e32 v[146:147], v[180:181]
	v_mov_b64_e32 v[148:149], v[182:183]
	v_mov_b64_e32 v[142:143], v[184:185]
	v_mov_b64_e32 v[144:145], v[186:187]
	v_add_u32_e32 v188, 0x20, v130
	v_ashrrev_i32_e32 v189, 31, v188
	v_lshlrev_b64 v[188:189], s66, v[188:189]
	v_lshl_add_u64 v[188:189], v[188:189], 3, v[134:135]
	global_load_dwordx4 v[172:175], v[188:189], off offset:48
	global_load_dwordx4 v[176:179], v[188:189], off offset:32
	global_load_dwordx4 v[180:183], v[188:189], off offset:16
	global_load_dwordx4 v[184:187], v[188:189], off
	v_pk_mul_f32 v[160:161], v[160:161], v[164:165]
	v_mul_f32_e32 v166, v108, v162
	v_mul_f32_e32 v168, v100, v163
	v_mov_b32_e32 v141, v144
	v_mov_b32_e32 v144, v143
	v_mov_b32_e32 v140, v142
	v_pk_mul_f32 v[154:155], v[102:103], v[144:145]
	v_pk_mul_f32 v[142:143], v[110:111], v[144:145]
	v_mov_b32_e32 v145, v148
	v_mov_b32_e32 v148, v147
	v_mov_b32_e32 v144, v146
	v_pk_mul_f32 v[156:157], v[104:105], v[148:149]
	v_pk_mul_f32 v[146:147], v[112:113], v[148:149]
	v_mov_b32_e32 v149, v152
	v_mov_b32_e32 v152, v151
	v_mov_b32_e32 v148, v150
	v_pk_mul_f32 v[150:151], v[98:99], v[152:153]
	v_mov_b32_e32 v167, v160
	v_mov_b32_e32 v169, v161
	v_pk_fma_f32 v[160:161], v[110:111], v[140:141], v[154:155] neg_lo:[0,0,1] neg_hi:[0,0,1]
	v_pk_fma_f32 v[154:155], v[106:107], v[148:149], v[150:151] neg_lo:[0,0,1] neg_hi:[0,0,1]
	v_pk_add_f32 v[150:151], v[166:167], v[168:169] neg_lo:[0,1] neg_hi:[0,1]
	v_mov_b32_e32 v166, v101
	v_mov_b32_e32 v167, v109
	v_pk_mul_f32 v[164:165], v[166:167], v[164:165]
	v_pk_mul_f32 v[152:153], v[106:107], v[152:153]
	v_mul_f32_e32 v158, v100, v162
	v_mul_f32_e32 v162, v108, v163
	v_mov_b32_e32 v159, v164
	v_mov_b32_e32 v163, v165
	v_pk_fma_f32 v[156:157], v[112:113], v[144:145], v[156:157] neg_lo:[0,0,1] neg_hi:[0,0,1]
	v_pk_fma_f32 v[164:165], v[102:103], v[140:141], v[142:143]
	v_pk_fma_f32 v[144:145], v[104:105], v[144:145], v[146:147]
	v_pk_fma_f32 v[142:143], v[98:99], v[148:149], v[152:153]
	v_pk_add_f32 v[140:141], v[158:159], v[162:163]
	s_branch .LBB0_3372

.LBB0_3376:
	s_mov_b32 s57, s56
	v_pk_mul_f32 v[138:139], s[56:57], v[160:161]
	s_and_b64 vcc, exec, s[4:5]
	v_cvt_pk_bf16_f32 v152, v138, v139
	v_pk_mul_f32 v[138:139], s[56:57], v[156:157]
	s_nop 0
	v_cvt_pk_bf16_f32 v153, v138, v139
	v_pk_mul_f32 v[138:139], s[56:57], v[154:155]
	s_nop 0
	v_cvt_pk_bf16_f32 v154, v138, v139
	v_pk_mul_f32 v[138:139], s[56:57], v[150:151]
	s_nop 0
	v_cvt_pk_bf16_f32 v155, v138, v139
	v_pk_mul_f32 v[138:139], s[56:57], v[164:165]
	s_nop 0
	v_cvt_pk_bf16_f32 v148, v138, v139
	v_pk_mul_f32 v[138:139], s[56:57], v[144:145]
	s_nop 0
	v_cvt_pk_bf16_f32 v149, v138, v139
	v_pk_mul_f32 v[138:139], s[56:57], v[142:143]
	s_nop 0
	v_cvt_pk_bf16_f32 v150, v138, v139
	v_pk_mul_f32 v[138:139], s[56:57], v[140:141]
	s_nop 0
	v_cvt_pk_bf16_f32 v151, v138, v139
	v_lshl_add_u64 v[138:139], v[146:147], 1, s[54:55]
	global_store_dwordx4 v[138:139], v[152:155], off
	v_lshl_add_u64 v[138:139], v[138:139], 0, s[92:93]
	global_store_dwordx4 v[138:139], v[148:151], off
	v_or_b32_e32 v138, 32, v130
	v_ashrrev_i32_e32 v139, 31, v138
	s_cbranch_vccnz .LBB0_3378
	v_lshlrev_b64 v[140:141], s66, v[138:139]
	v_lshl_add_u64 v[140:141], v[140:141], 3, v[134:135]
	v_mov_b32_e32 v160, v93
	v_mov_b32_e32 v161, v85
	s_waitcnt vmcnt(2)
	v_mov_b64_e32 v[162:163], v[172:173]
	v_mov_b64_e32 v[164:165], v[174:175]
	v_mov_b64_e32 v[150:151], v[176:177]
	v_mov_b64_e32 v[152:153], v[178:179]
	v_mov_b64_e32 v[146:147], v[180:181]
	v_mov_b64_e32 v[148:149], v[182:183]
	v_mov_b64_e32 v[142:143], v[184:185]
	v_mov_b64_e32 v[144:145], v[186:187]
	v_add_u32_e32 v188, 0x30, v130
	v_ashrrev_i32_e32 v189, 31, v188
	v_lshlrev_b64 v[188:189], s66, v[188:189]
	v_lshl_add_u64 v[188:189], v[188:189], 3, v[134:135]
	global_load_dwordx4 v[172:175], v[188:189], off offset:48
	global_load_dwordx4 v[176:179], v[188:189], off offset:32
	global_load_dwordx4 v[180:183], v[188:189], off offset:16
	global_load_dwordx4 v[184:187], v[188:189], off
	v_pk_mul_f32 v[160:161], v[160:161], v[164:165]
	s_nop 0
	v_mov_b32_e32 v169, v160
	v_mov_b32_e32 v171, v161
	v_mov_b32_e32 v141, v144
	v_mov_b32_e32 v144, v143
	v_mov_b32_e32 v140, v142
	v_pk_mul_f32 v[156:157], v[86:87], v[144:145]
	v_pk_mul_f32 v[142:143], v[94:95], v[144:145]
	v_mov_b32_e32 v145, v148
	v_mov_b32_e32 v148, v147
	v_mov_b32_e32 v144, v146
	v_pk_mul_f32 v[158:159], v[88:89], v[148:149]
	v_pk_mul_f32 v[146:147], v[96:97], v[148:149]
	v_mov_b32_e32 v149, v152
	v_mov_b32_e32 v152, v151
	v_mov_b32_e32 v148, v150
	v_pk_mul_f32 v[166:167], v[82:83], v[152:153]
	v_pk_fma_f32 v[160:161], v[96:97], v[144:145], v[158:159] neg_lo:[0,0,1] neg_hi:[0,0,1]
	v_pk_fma_f32 v[158:159], v[90:91], v[148:149], v[166:167] neg_lo:[0,0,1] neg_hi:[0,0,1]
	v_mov_b32_e32 v166, v85
	v_mov_b32_e32 v167, v93
	v_pk_mul_f32 v[164:165], v[166:167], v[164:165]
	v_pk_mul_f32 v[150:151], v[90:91], v[152:153]
	v_mul_f32_e32 v168, v92, v162
	v_mul_f32_e32 v170, v84, v163
	v_mul_f32_e32 v152, v84, v162
	v_mul_f32_e32 v154, v92, v163
	v_mov_b32_e32 v153, v164
	v_mov_b32_e32 v155, v165
	v_pk_fma_f32 v[162:163], v[94:95], v[140:141], v[156:157] neg_lo:[0,0,1] neg_hi:[0,0,1]
	v_pk_add_f32 v[156:157], v[168:169], v[170:171] neg_lo:[0,1] neg_hi:[0,1]
	v_pk_fma_f32 v[164:165], v[86:87], v[140:141], v[142:143]
	v_pk_fma_f32 v[144:145], v[88:89], v[144:145], v[146:147]
	v_pk_fma_f32 v[142:143], v[82:83], v[148:149], v[150:151]
	v_pk_add_f32 v[140:141], v[152:153], v[154:155]
	s_and_b64 vcc, exec, s[6:7]
	s_mov_b64 s[60:61], -1
	s_cbranch_vccz .LBB0_3379
	s_branch .LBB0_3380

.LBB0_3382:
	v_pk_mul_f32 v[138:139], s[56:57], v[162:163]
	s_and_b64 vcc, exec, s[4:5]
	v_cvt_pk_bf16_f32 v148, v138, v139
	v_pk_mul_f32 v[138:139], s[56:57], v[160:161]
	s_nop 0
	v_cvt_pk_bf16_f32 v149, v138, v139
	v_pk_mul_f32 v[138:139], s[56:57], v[158:159]
	s_nop 0
	v_cvt_pk_bf16_f32 v150, v138, v139
	v_pk_mul_f32 v[138:139], s[56:57], v[156:157]
	s_nop 0
	v_cvt_pk_bf16_f32 v151, v138, v139
	v_pk_mul_f32 v[138:139], s[56:57], v[164:165]
	s_nop 0
	v_cvt_pk_bf16_f32 v152, v138, v139
	v_pk_mul_f32 v[138:139], s[56:57], v[144:145]
	s_nop 0
	v_cvt_pk_bf16_f32 v153, v138, v139
	v_pk_mul_f32 v[138:139], s[56:57], v[142:143]
	s_nop 0
	v_cvt_pk_bf16_f32 v154, v138, v139
	v_pk_mul_f32 v[138:139], s[56:57], v[140:141]
	s_nop 0
	v_cvt_pk_bf16_f32 v155, v138, v139
	v_lshl_add_u64 v[138:139], v[146:147], 1, s[54:55]
	global_store_dwordx4 v[138:139], v[148:151], off
	v_lshl_add_u64 v[138:139], v[138:139], 0, s[92:93]
	global_store_dwordx4 v[138:139], v[152:155], off
	v_or_b32_e32 v138, 48, v130
	v_ashrrev_i32_e32 v139, 31, v138
	s_cbranch_vccnz .LBB0_3384
	v_lshlrev_b64 v[140:141], s66, v[138:139]
	v_lshl_add_u64 v[140:141], v[140:141], 3, v[134:135]
	v_mov_b32_e32 v160, v77
	v_mov_b32_e32 v161, v69
	s_waitcnt vmcnt(2)
	v_mov_b64_e32 v[162:163], v[172:173]
	v_mov_b64_e32 v[164:165], v[174:175]
	v_mov_b64_e32 v[150:151], v[176:177]
	v_mov_b64_e32 v[152:153], v[178:179]
	v_mov_b64_e32 v[146:147], v[180:181]
	v_mov_b64_e32 v[148:149], v[182:183]
	v_mov_b64_e32 v[142:143], v[184:185]
	v_mov_b64_e32 v[144:145], v[186:187]
	v_add_u32_e32 v188, 0x80, v130
	v_ashrrev_i32_e32 v189, 31, v188
	v_lshlrev_b64 v[188:189], s66, v[188:189]
	v_lshl_add_u64 v[188:189], v[188:189], 3, v[134:135]
	global_load_dwordx4 v[172:175], v[188:189], off offset:48
	global_load_dwordx4 v[176:179], v[188:189], off offset:32
	global_load_dwordx4 v[180:183], v[188:189], off offset:16
	global_load_dwordx4 v[184:187], v[188:189], off
	v_pk_mul_f32 v[160:161], v[160:161], v[164:165]
	s_nop 0
	v_mov_b32_e32 v169, v160
	v_mov_b32_e32 v171, v161
	v_mov_b32_e32 v141, v144
	v_mov_b32_e32 v144, v143
	v_mov_b32_e32 v140, v142
	v_pk_mul_f32 v[156:157], v[70:71], v[144:145]
	v_pk_mul_f32 v[142:143], v[78:79], v[144:145]
	v_mov_b32_e32 v145, v148
	v_mov_b32_e32 v148, v147
	v_mov_b32_e32 v144, v146
	v_pk_mul_f32 v[158:159], v[72:73], v[148:149]
	v_pk_mul_f32 v[146:147], v[80:81], v[148:149]
	v_mov_b32_e32 v149, v152
	v_mov_b32_e32 v152, v151
	v_mov_b32_e32 v148, v150
	v_pk_mul_f32 v[166:167], v[66:67], v[152:153]
	v_pk_fma_f32 v[160:161], v[80:81], v[144:145], v[158:159] neg_lo:[0,0,1] neg_hi:[0,0,1]
	v_pk_fma_f32 v[158:159], v[74:75], v[148:149], v[166:167] neg_lo:[0,0,1] neg_hi:[0,0,1]
	v_mov_b32_e32 v166, v69
	v_mov_b32_e32 v167, v77
	v_pk_mul_f32 v[164:165], v[166:167], v[164:165]
	v_pk_mul_f32 v[150:151], v[74:75], v[152:153]
	v_mul_f32_e32 v168, v76, v162
	v_mul_f32_e32 v170, v68, v163
	v_mul_f32_e32 v152, v68, v162
	v_mul_f32_e32 v154, v76, v163
	v_mov_b32_e32 v153, v164
	v_mov_b32_e32 v155, v165
	v_pk_fma_f32 v[162:163], v[78:79], v[140:141], v[156:157] neg_lo:[0,0,1] neg_hi:[0,0,1]
	v_pk_add_f32 v[156:157], v[168:169], v[170:171] neg_lo:[0,1] neg_hi:[0,1]
	v_pk_fma_f32 v[164:165], v[70:71], v[140:141], v[142:143]
	v_pk_fma_f32 v[144:145], v[72:73], v[144:145], v[146:147]
	v_pk_fma_f32 v[142:143], v[66:67], v[148:149], v[150:151]
	v_pk_add_f32 v[140:141], v[152:153], v[154:155]
	s_and_b64 vcc, exec, s[6:7]
	s_mov_b64 s[60:61], -1
	s_cbranch_vccz .LBB0_3385
	s_branch .LBB0_3386

.LBB0_3388:
	v_pk_mul_f32 v[138:139], s[56:57], v[162:163]
	s_and_b64 vcc, exec, s[4:5]
	v_cvt_pk_bf16_f32 v148, v138, v139
	v_pk_mul_f32 v[138:139], s[56:57], v[160:161]
	s_nop 0
	v_cvt_pk_bf16_f32 v149, v138, v139
	v_pk_mul_f32 v[138:139], s[56:57], v[158:159]
	s_nop 0
	v_cvt_pk_bf16_f32 v150, v138, v139
	v_pk_mul_f32 v[138:139], s[56:57], v[156:157]
	s_nop 0
	v_cvt_pk_bf16_f32 v151, v138, v139
	v_pk_mul_f32 v[138:139], s[56:57], v[164:165]
	s_nop 0
	v_cvt_pk_bf16_f32 v152, v138, v139
	v_pk_mul_f32 v[138:139], s[56:57], v[144:145]
	s_nop 0
	v_cvt_pk_bf16_f32 v153, v138, v139
	v_pk_mul_f32 v[138:139], s[56:57], v[142:143]
	s_nop 0
	v_cvt_pk_bf16_f32 v154, v138, v139
	v_pk_mul_f32 v[138:139], s[56:57], v[140:141]
	s_nop 0
	v_cvt_pk_bf16_f32 v155, v138, v139
	v_lshl_add_u64 v[138:139], v[146:147], 1, s[54:55]
	global_store_dwordx4 v[138:139], v[148:151], off
	v_lshl_add_u64 v[138:139], v[138:139], 0, s[92:93]
	global_store_dwordx4 v[138:139], v[152:155], off
	v_add_u32_e32 v138, 0x80, v130
	v_ashrrev_i32_e32 v139, 31, v138
	s_cbranch_vccnz .LBB0_3390
	v_lshlrev_b64 v[140:141], s66, v[138:139]
	v_lshl_add_u64 v[140:141], v[140:141], 3, v[134:135]
	v_mov_b32_e32 v160, v61
	v_mov_b32_e32 v161, v53
	s_waitcnt vmcnt(2)
	v_mov_b64_e32 v[162:163], v[172:173]
	v_mov_b64_e32 v[164:165], v[174:175]
	v_mov_b64_e32 v[150:151], v[176:177]
	v_mov_b64_e32 v[152:153], v[178:179]
	v_mov_b64_e32 v[146:147], v[180:181]
	v_mov_b64_e32 v[148:149], v[182:183]
	v_mov_b64_e32 v[142:143], v[184:185]
	v_mov_b64_e32 v[144:145], v[186:187]
	v_add_u32_e32 v188, 0x90, v130
	v_ashrrev_i32_e32 v189, 31, v188
	v_lshlrev_b64 v[188:189], s66, v[188:189]
	v_lshl_add_u64 v[188:189], v[188:189], 3, v[134:135]
	global_load_dwordx4 v[172:175], v[188:189], off offset:48
	global_load_dwordx4 v[176:179], v[188:189], off offset:32
	global_load_dwordx4 v[180:183], v[188:189], off offset:16
	global_load_dwordx4 v[184:187], v[188:189], off
	v_pk_mul_f32 v[160:161], v[160:161], v[164:165]
	v_mul_f32_e32 v166, v60, v162
	v_mul_f32_e32 v168, v52, v163
	v_mov_b32_e32 v141, v144
	v_mov_b32_e32 v144, v143
	v_mov_b32_e32 v140, v142
	v_pk_mul_f32 v[154:155], v[54:55], v[144:145]
	v_pk_mul_f32 v[142:143], v[62:63], v[144:145]
	v_mov_b32_e32 v145, v148
	v_mov_b32_e32 v148, v147
	v_mov_b32_e32 v144, v146
	v_pk_mul_f32 v[156:157], v[56:57], v[148:149]
	v_pk_mul_f32 v[146:147], v[64:65], v[148:149]
	v_mov_b32_e32 v149, v152
	v_mov_b32_e32 v152, v151
	v_mov_b32_e32 v148, v150
	v_pk_mul_f32 v[150:151], v[50:51], v[152:153]
	v_mov_b32_e32 v167, v160
	v_mov_b32_e32 v169, v161
	v_pk_fma_f32 v[160:161], v[62:63], v[140:141], v[154:155] neg_lo:[0,0,1] neg_hi:[0,0,1]
	v_pk_fma_f32 v[154:155], v[58:59], v[148:149], v[150:151] neg_lo:[0,0,1] neg_hi:[0,0,1]
	v_pk_add_f32 v[150:151], v[166:167], v[168:169] neg_lo:[0,1] neg_hi:[0,1]
	v_mov_b32_e32 v166, v53
	v_mov_b32_e32 v167, v61
	v_pk_mul_f32 v[164:165], v[166:167], v[164:165]
	v_pk_mul_f32 v[152:153], v[58:59], v[152:153]
	v_mul_f32_e32 v158, v52, v162
	v_mul_f32_e32 v162, v60, v163
	v_mov_b32_e32 v159, v164
	v_mov_b32_e32 v163, v165
	v_pk_fma_f32 v[156:157], v[64:65], v[144:145], v[156:157] neg_lo:[0,0,1] neg_hi:[0,0,1]
	v_pk_fma_f32 v[164:165], v[54:55], v[140:141], v[142:143]
	v_pk_fma_f32 v[144:145], v[56:57], v[144:145], v[146:147]
	v_pk_fma_f32 v[142:143], v[50:51], v[148:149], v[152:153]
	v_pk_add_f32 v[140:141], v[158:159], v[162:163]
	s_and_b64 vcc, exec, s[6:7]
	s_mov_b64 s[60:61], -1
	s_cbranch_vccz .LBB0_3391
	s_branch .LBB0_3392

.LBB0_3394:
	v_pk_mul_f32 v[138:139], s[56:57], v[160:161]
	s_and_b64 vcc, exec, s[4:5]
	v_cvt_pk_bf16_f32 v152, v138, v139
	v_pk_mul_f32 v[138:139], s[56:57], v[156:157]
	s_movk_i32 s64, 0x1800
	v_cvt_pk_bf16_f32 v153, v138, v139
	v_pk_mul_f32 v[138:139], s[56:57], v[154:155]
	s_nop 0
	v_cvt_pk_bf16_f32 v154, v138, v139
	v_pk_mul_f32 v[138:139], s[56:57], v[150:151]
	s_nop 0
	v_cvt_pk_bf16_f32 v155, v138, v139
	v_pk_mul_f32 v[138:139], s[56:57], v[164:165]
	s_nop 0
	v_cvt_pk_bf16_f32 v148, v138, v139
	v_pk_mul_f32 v[138:139], s[56:57], v[144:145]
	s_nop 0
	v_cvt_pk_bf16_f32 v149, v138, v139
	v_pk_mul_f32 v[138:139], s[56:57], v[142:143]
	s_nop 0
	v_cvt_pk_bf16_f32 v150, v138, v139
	v_pk_mul_f32 v[138:139], s[56:57], v[140:141]
	s_nop 0
	v_cvt_pk_bf16_f32 v151, v138, v139
	v_lshl_add_u64 v[138:139], v[146:147], 1, s[54:55]
	global_store_dwordx4 v[138:139], v[152:155], off
	v_lshl_add_u64 v[138:139], v[138:139], 0, s[92:93]
	global_store_dwordx4 v[138:139], v[148:151], off
	v_add_u32_e32 v138, 0x90, v130
	v_ashrrev_i32_e32 v139, 31, v138
	s_cbranch_vccnz .LBB0_3396
	v_lshlrev_b64 v[140:141], s66, v[138:139]
	v_lshl_add_u64 v[140:141], v[140:141], 3, v[134:135]
	v_mov_b32_e32 v160, v45
	v_mov_b32_e32 v161, v37
	s_waitcnt vmcnt(2)
	v_mov_b64_e32 v[162:163], v[172:173]
	v_mov_b64_e32 v[164:165], v[174:175]
	v_mov_b64_e32 v[150:151], v[176:177]
	v_mov_b64_e32 v[152:153], v[178:179]
	v_mov_b64_e32 v[146:147], v[180:181]
	v_mov_b64_e32 v[148:149], v[182:183]
	v_mov_b64_e32 v[142:143], v[184:185]
	v_mov_b64_e32 v[144:145], v[186:187]
	v_add_u32_e32 v188, 0xa0, v130
	v_ashrrev_i32_e32 v189, 31, v188
	v_lshlrev_b64 v[188:189], s66, v[188:189]
	v_lshl_add_u64 v[188:189], v[188:189], 3, v[134:135]
	global_load_dwordx4 v[172:175], v[188:189], off offset:48
	global_load_dwordx4 v[176:179], v[188:189], off offset:32
	global_load_dwordx4 v[180:183], v[188:189], off offset:16
	global_load_dwordx4 v[184:187], v[188:189], off
	v_pk_mul_f32 v[160:161], v[160:161], v[164:165]
	s_nop 0
	v_mov_b32_e32 v169, v160
	v_mov_b32_e32 v171, v161
	v_mov_b32_e32 v141, v144
	v_mov_b32_e32 v144, v143
	v_mov_b32_e32 v140, v142
	v_pk_mul_f32 v[156:157], v[38:39], v[144:145]
	v_pk_mul_f32 v[142:143], v[46:47], v[144:145]
	v_mov_b32_e32 v145, v148
	v_mov_b32_e32 v148, v147
	v_mov_b32_e32 v144, v146
	v_pk_mul_f32 v[158:159], v[40:41], v[148:149]
	v_pk_mul_f32 v[146:147], v[48:49], v[148:149]
	v_mov_b32_e32 v149, v152
	v_mov_b32_e32 v152, v151
	v_mov_b32_e32 v148, v150
	v_pk_mul_f32 v[166:167], v[34:35], v[152:153]
	v_pk_fma_f32 v[160:161], v[48:49], v[144:145], v[158:159] neg_lo:[0,0,1] neg_hi:[0,0,1]
	v_pk_fma_f32 v[158:159], v[42:43], v[148:149], v[166:167] neg_lo:[0,0,1] neg_hi:[0,0,1]
	v_mov_b32_e32 v166, v37
	v_mov_b32_e32 v167, v45
	v_pk_mul_f32 v[164:165], v[166:167], v[164:165]
	v_pk_mul_f32 v[150:151], v[42:43], v[152:153]
	v_mul_f32_e32 v168, v44, v162
	v_mul_f32_e32 v170, v36, v163
	v_mul_f32_e32 v152, v36, v162
	v_mul_f32_e32 v154, v44, v163
	v_mov_b32_e32 v153, v164
	v_mov_b32_e32 v155, v165
	v_pk_fma_f32 v[162:163], v[46:47], v[140:141], v[156:157] neg_lo:[0,0,1] neg_hi:[0,0,1]
	v_pk_add_f32 v[156:157], v[168:169], v[170:171] neg_lo:[0,1] neg_hi:[0,1]
	v_pk_fma_f32 v[164:165], v[38:39], v[140:141], v[142:143]
	v_pk_fma_f32 v[144:145], v[40:41], v[144:145], v[146:147]
	v_pk_fma_f32 v[142:143], v[34:35], v[148:149], v[150:151]
	v_pk_add_f32 v[140:141], v[152:153], v[154:155]
	s_and_b64 vcc, exec, s[6:7]
	s_mov_b64 s[60:61], -1
	s_cbranch_vccz .LBB0_3397
	s_branch .LBB0_3398

.LBB0_3400:
	v_pk_mul_f32 v[138:139], s[56:57], v[162:163]
	s_and_b64 vcc, exec, s[4:5]
	v_cvt_pk_bf16_f32 v148, v138, v139
	v_pk_mul_f32 v[138:139], s[56:57], v[160:161]
	s_nop 0
	v_cvt_pk_bf16_f32 v149, v138, v139
	v_pk_mul_f32 v[138:139], s[56:57], v[158:159]
	s_nop 0
	v_cvt_pk_bf16_f32 v150, v138, v139
	v_pk_mul_f32 v[138:139], s[56:57], v[156:157]
	s_nop 0
	v_cvt_pk_bf16_f32 v151, v138, v139
	v_pk_mul_f32 v[138:139], s[56:57], v[164:165]
	s_nop 0
	v_cvt_pk_bf16_f32 v152, v138, v139
	v_pk_mul_f32 v[138:139], s[56:57], v[144:145]
	s_nop 0
	v_cvt_pk_bf16_f32 v153, v138, v139
	v_pk_mul_f32 v[138:139], s[56:57], v[142:143]
	s_nop 0
	v_cvt_pk_bf16_f32 v154, v138, v139
	v_pk_mul_f32 v[138:139], s[56:57], v[140:141]
	s_nop 0
	v_cvt_pk_bf16_f32 v155, v138, v139
	v_lshl_add_u64 v[138:139], v[146:147], 1, s[54:55]
	global_store_dwordx4 v[138:139], v[148:151], off
	v_lshl_add_u64 v[138:139], v[138:139], 0, s[92:93]
	global_store_dwordx4 v[138:139], v[152:155], off
	v_add_u32_e32 v138, 0xa0, v130
	v_ashrrev_i32_e32 v139, 31, v138
	s_cbranch_vccnz .LBB0_3402
	v_lshlrev_b64 v[140:141], s66, v[138:139]
	v_lshl_add_u64 v[140:141], v[140:141], 3, v[134:135]
	v_mov_b32_e32 v160, v29
	v_mov_b32_e32 v161, v21
	s_waitcnt vmcnt(2)
	v_mov_b64_e32 v[162:163], v[172:173]
	v_mov_b64_e32 v[164:165], v[174:175]
	v_mov_b64_e32 v[150:151], v[176:177]
	v_mov_b64_e32 v[152:153], v[178:179]
	v_mov_b64_e32 v[146:147], v[180:181]
	v_mov_b64_e32 v[148:149], v[182:183]
	v_mov_b64_e32 v[142:143], v[184:185]
	v_mov_b64_e32 v[144:145], v[186:187]
	v_add_u32_e32 v188, 0xb0, v130
	v_ashrrev_i32_e32 v189, 31, v188
	v_lshlrev_b64 v[188:189], s66, v[188:189]
	v_lshl_add_u64 v[188:189], v[188:189], 3, v[134:135]
	global_load_dwordx4 v[172:175], v[188:189], off offset:48
	global_load_dwordx4 v[176:179], v[188:189], off offset:32
	global_load_dwordx4 v[180:183], v[188:189], off offset:16
	global_load_dwordx4 v[184:187], v[188:189], off
	v_pk_mul_f32 v[160:161], v[160:161], v[164:165]
	s_nop 0
	v_mov_b32_e32 v169, v160
	v_mov_b32_e32 v171, v161
	v_mov_b32_e32 v141, v144
	v_mov_b32_e32 v144, v143
	v_mov_b32_e32 v140, v142
	v_pk_mul_f32 v[156:157], v[22:23], v[144:145]
	v_pk_mul_f32 v[142:143], v[30:31], v[144:145]
	v_mov_b32_e32 v145, v148
	v_mov_b32_e32 v148, v147
	v_mov_b32_e32 v144, v146
	v_pk_mul_f32 v[158:159], v[24:25], v[148:149]
	v_pk_mul_f32 v[146:147], v[32:33], v[148:149]
	v_mov_b32_e32 v149, v152
	v_mov_b32_e32 v152, v151
	v_mov_b32_e32 v148, v150
	v_pk_mul_f32 v[166:167], v[18:19], v[152:153]
	v_pk_fma_f32 v[160:161], v[32:33], v[144:145], v[158:159] neg_lo:[0,0,1] neg_hi:[0,0,1]
	v_pk_fma_f32 v[158:159], v[26:27], v[148:149], v[166:167] neg_lo:[0,0,1] neg_hi:[0,0,1]
	v_mov_b32_e32 v166, v21
	v_mov_b32_e32 v167, v29
	v_pk_mul_f32 v[164:165], v[166:167], v[164:165]
	v_pk_mul_f32 v[150:151], v[26:27], v[152:153]
	v_mul_f32_e32 v168, v28, v162
	v_mul_f32_e32 v170, v20, v163
	v_mul_f32_e32 v152, v20, v162
	v_mul_f32_e32 v154, v28, v163
	v_mov_b32_e32 v153, v164
	v_mov_b32_e32 v155, v165
	v_pk_fma_f32 v[162:163], v[30:31], v[140:141], v[156:157] neg_lo:[0,0,1] neg_hi:[0,0,1]
	v_pk_add_f32 v[156:157], v[168:169], v[170:171] neg_lo:[0,1] neg_hi:[0,1]
	v_pk_fma_f32 v[164:165], v[22:23], v[140:141], v[142:143]
	v_pk_fma_f32 v[144:145], v[24:25], v[144:145], v[146:147]
	v_pk_fma_f32 v[142:143], v[18:19], v[148:149], v[150:151]
	v_pk_add_f32 v[140:141], v[152:153], v[154:155]
	s_and_b64 vcc, exec, s[6:7]
	s_mov_b64 s[60:61], -1
	s_cbranch_vccz .LBB0_3403
	s_branch .LBB0_3404

.LBB0_3406:
	v_pk_mul_f32 v[138:139], s[56:57], v[162:163]
	s_and_b64 vcc, exec, s[4:5]
	v_cvt_pk_bf16_f32 v148, v138, v139
	v_pk_mul_f32 v[138:139], s[56:57], v[160:161]
	s_mov_b64 s[60:61], 0x400
	v_cvt_pk_bf16_f32 v149, v138, v139
	v_pk_mul_f32 v[138:139], s[56:57], v[158:159]
	s_nop 0
	v_cvt_pk_bf16_f32 v150, v138, v139
	v_pk_mul_f32 v[138:139], s[56:57], v[156:157]
	s_nop 0
	v_cvt_pk_bf16_f32 v151, v138, v139
	v_pk_mul_f32 v[138:139], s[56:57], v[164:165]
	s_nop 0
	v_cvt_pk_bf16_f32 v152, v138, v139
	v_pk_mul_f32 v[138:139], s[56:57], v[144:145]
	s_nop 0
	v_cvt_pk_bf16_f32 v153, v138, v139
	v_pk_mul_f32 v[138:139], s[56:57], v[142:143]
	s_nop 0
	v_cvt_pk_bf16_f32 v154, v138, v139
	v_pk_mul_f32 v[138:139], s[56:57], v[140:141]
	s_nop 0
	v_cvt_pk_bf16_f32 v155, v138, v139
	v_lshl_add_u64 v[138:139], v[146:147], 1, s[54:55]
	global_store_dwordx4 v[138:139], v[148:151], off
	v_lshl_add_u64 v[138:139], v[138:139], 0, s[92:93]
	global_store_dwordx4 v[138:139], v[152:155], off
	v_add_u32_e32 v138, 0xb0, v130
	v_ashrrev_i32_e32 v139, 31, v138
	s_cbranch_vccnz .LBB0_3408
	v_lshlrev_b64 v[140:141], s66, v[138:139]
	v_lshl_add_u64 v[134:135], v[140:141], 3, v[134:135]
	v_mov_b32_e32 v158, v13
	v_mov_b32_e32 v159, v5
	s_waitcnt vmcnt(2)
	v_mov_b64_e32 v[160:161], v[172:173]
	v_mov_b64_e32 v[162:163], v[174:175]
	v_mov_b64_e32 v[148:149], v[176:177]
	v_mov_b64_e32 v[150:151], v[178:179]
	v_mov_b64_e32 v[144:145], v[180:181]
	v_mov_b64_e32 v[146:147], v[182:183]
	v_mov_b64_e32 v[140:141], v[184:185]
	v_mov_b64_e32 v[142:143], v[186:187]
	v_pk_mul_f32 v[158:159], v[158:159], v[162:163]
	v_mul_f32_e32 v164, v12, v160
	v_mul_f32_e32 v166, v4, v161
	v_mov_b32_e32 v135, v142
	v_mov_b32_e32 v142, v141
	v_mov_b32_e32 v134, v140
	v_pk_mul_f32 v[152:153], v[6:7], v[142:143]
	v_pk_mul_f32 v[140:141], v[14:15], v[142:143]
	v_mov_b32_e32 v143, v146
	v_mov_b32_e32 v146, v145
	v_mov_b32_e32 v142, v144
	v_pk_mul_f32 v[154:155], v[8:9], v[146:147]
	v_pk_mul_f32 v[144:145], v[16:17], v[146:147]
	v_mov_b32_e32 v147, v150
	v_mov_b32_e32 v150, v149
	v_mov_b32_e32 v146, v148
	v_pk_mul_f32 v[148:149], v[2:3], v[150:151]
	v_mov_b32_e32 v165, v158
	v_mov_b32_e32 v167, v159
	v_pk_fma_f32 v[158:159], v[14:15], v[134:135], v[152:153] neg_lo:[0,0,1] neg_hi:[0,0,1]
	v_pk_fma_f32 v[152:153], v[10:11], v[146:147], v[148:149] neg_lo:[0,0,1] neg_hi:[0,0,1]
	v_pk_add_f32 v[148:149], v[164:165], v[166:167] neg_lo:[0,1] neg_hi:[0,1]
	v_mov_b32_e32 v164, v5
	v_mov_b32_e32 v165, v13
	v_pk_mul_f32 v[162:163], v[164:165], v[162:163]
	v_pk_mul_f32 v[150:151], v[10:11], v[150:151]
	v_mul_f32_e32 v156, v4, v160
	v_mul_f32_e32 v160, v12, v161
	v_mov_b32_e32 v157, v162
	v_mov_b32_e32 v161, v163
	v_pk_fma_f32 v[154:155], v[16:17], v[142:143], v[154:155] neg_lo:[0,0,1] neg_hi:[0,0,1]
	v_pk_fma_f32 v[162:163], v[6:7], v[134:135], v[140:141]
	v_pk_fma_f32 v[142:143], v[8:9], v[142:143], v[144:145]
	v_pk_fma_f32 v[140:141], v[2:3], v[146:147], v[150:151]
	v_pk_add_f32 v[134:135], v[156:157], v[160:161]
	s_branch .LBB0_3409
